# adds P9/P10: unit bias vectors loaded at unit start (epilogue no longer waits vmcnt(0)); P9 token loads issued together
# speedup vs baseline: 1.0028x; 1.0028x over previous
; template <class Epi, class Sched, bool ALIGN_EPI = false, bool SP2 = false, bool F8 = false, bool GATHER = false>
; __device__ __forceinline__ void gemm_phase(PG8_LAS unsigned char* lds, const Gemm g, const Sched& S, const Epi& E) {
;     ...
; #pragma unroll
;         for (int a = 0; a < 2; ++a)
; #pragma unroll
;             for (int b = 0; b < 2; ++b)
; #pragma unroll
;                 for (int m = 0; m < 4; ++m)
; #pragma unroll
;                     for (int n = 0; n < 2; ++n) acc[a][b][m][n] = (f32x4){0.f, 0.f, 0.f, 0.f};
;     __device__ __forceinline__ void operator()(const f32x4 (&acc)[2][2][4][2], const Unit& u, int wr, int wc, int fr, int fq) const {
;         const int e = u.pn >> 4, pnl = u.pn & 15; const int row0 = u.pm * BM + wr * 64 + fr; const int col0 = pnl * HALF + wc * 32 + 8 * fq;
;         f32x4 bgv[2], buv[2];
; #pragma unroll
;         for (int n = 0; n < 2; ++n) { bgv[n] = *(const f32x4*)(bg + (size_t)e * 2048 + col0 + 4 * n); buv[n] = *(const f32x4*)(bu + (size_t)e * 2048 + col0 + 4 * n); }
.LBB0_995:
	s_ashr_i32 s98, s46, 4
	s_lshl_b32 s100, s46, 7
	s_ashr_i32 s99, s98, 31
	s_and_b32 s100, s100, 0x780
	s_lshl_b64 s[98:99], s[98:99], 13
	v_or_b32_e32 v2, s100, v195
	v_lshlrev_b32_e32 v2, 2, v2
	s_add_u32 s100, s16, s98
	s_addc_u32 s101, s17, s99
	global_load_dwordx4 v[240:243], v2, s[100:101]
	global_load_dwordx4 v[248:251], v2, s[100:101] offset:16
	s_add_u32 s98, s20, s98
	s_addc_u32 s99, s21, s99
	global_load_dwordx4 v[252:255], v2, s[98:99]
	global_load_dwordx2 v[244:245], v2, s[98:99] offset:16
	global_load_dword v247, v2, s[98:99] offset:24
	global_load_dword v190, v2, s[98:99] offset:28
	s_ashr_i32 s43, s42, 31
	s_lshl_b64 s[44:45], s[42:43], 19
	s_add_u32 s44, s2, s44
	s_addc_u32 s45, s3, s45
	s_and_b64 s[50:51], s[50:51], exec
	s_cselect_b32 s43, s45, s49
	s_cselect_b32 s63, s44, s48
	v_mov_b32_e32 v169, v163
	v_mov_b32_e32 v173, v163
	s_add_u32 s64, s48, 0x100
	v_mov_b32_e32 v34, 0
	v_lshl_add_u64 v[174:175], s[36:37], 0, v[172:173]
	v_lshl_add_u64 v[176:177], s[36:37], 0, v[168:169]
	s_addc_u32 s65, s49, 0
	s_mov_b32 s66, -2
	s_mov_b64 s[48:49], 0
	v_mov_b32_e32 v35, v34
	v_mov_b32_e32 v36, v34
	v_mov_b32_e32 v37, v34
	v_mov_b32_e32 v42, v34
	v_mov_b32_e32 v43, v34
	v_mov_b32_e32 v44, v34
	v_mov_b32_e32 v45, v34
	v_mov_b32_e32 v50, v34
	v_mov_b32_e32 v51, v34
	v_mov_b32_e32 v52, v34
	v_mov_b32_e32 v53, v34
	v_mov_b32_e32 v58, v34
	v_mov_b32_e32 v59, v34
	v_mov_b32_e32 v60, v34
	v_mov_b32_e32 v61, v34
	v_mov_b32_e32 v66, v34
	v_mov_b32_e32 v67, v34
	v_mov_b32_e32 v68, v34
	v_mov_b32_e32 v69, v34
	v_mov_b32_e32 v74, v34
	v_mov_b32_e32 v75, v34
	v_mov_b32_e32 v76, v34
	v_mov_b32_e32 v77, v34
	v_mov_b32_e32 v82, v34
	v_mov_b32_e32 v83, v34
	v_mov_b32_e32 v84, v34
	v_mov_b32_e32 v85, v34
	v_mov_b32_e32 v90, v34
	v_mov_b32_e32 v91, v34
	v_mov_b32_e32 v92, v34
	v_mov_b32_e32 v93, v34
	v_mov_b32_e32 v38, v34
	v_mov_b32_e32 v39, v34
	v_mov_b32_e32 v40, v34
	v_mov_b32_e32 v41, v34
	v_mov_b32_e32 v46, v34
	v_mov_b32_e32 v47, v34
	v_mov_b32_e32 v48, v34
	v_mov_b32_e32 v49, v34
	v_mov_b32_e32 v54, v34
	v_mov_b32_e32 v55, v34
	v_mov_b32_e32 v56, v34
	v_mov_b32_e32 v57, v34
	v_mov_b32_e32 v62, v34
	v_mov_b32_e32 v63, v34
	v_mov_b32_e32 v64, v34
	v_mov_b32_e32 v65, v34
	v_mov_b32_e32 v70, v34
	v_mov_b32_e32 v71, v34
	v_mov_b32_e32 v72, v34
	v_mov_b32_e32 v73, v34
	v_mov_b32_e32 v78, v34
	v_mov_b32_e32 v79, v34
	v_mov_b32_e32 v80, v34
	v_mov_b32_e32 v81, v34
	v_mov_b32_e32 v86, v34
	v_mov_b32_e32 v87, v34
	v_mov_b32_e32 v88, v34
	v_mov_b32_e32 v89, v34
	v_mov_b32_e32 v94, v34
	v_mov_b32_e32 v95, v34
	v_mov_b32_e32 v96, v34
	v_mov_b32_e32 v97, v34
	v_mov_b32_e32 v98, v34
	v_mov_b32_e32 v99, v34
	v_mov_b32_e32 v100, v34
	v_mov_b32_e32 v101, v34
	v_mov_b32_e32 v106, v34
	v_mov_b32_e32 v107, v34
	v_mov_b32_e32 v108, v34
	v_mov_b32_e32 v109, v34
	v_mov_b32_e32 v114, v34
	v_mov_b32_e32 v115, v34
	v_mov_b32_e32 v116, v34
	v_mov_b32_e32 v117, v34
	v_mov_b32_e32 v122, v34
	v_mov_b32_e32 v123, v34
	v_mov_b32_e32 v124, v34
	v_mov_b32_e32 v125, v34
	v_mov_b32_e32 v130, v34
	v_mov_b32_e32 v131, v34
	v_mov_b32_e32 v132, v34
	v_mov_b32_e32 v133, v34
	v_mov_b32_e32 v138, v34
	v_mov_b32_e32 v139, v34
	v_mov_b32_e32 v140, v34
	v_mov_b32_e32 v141, v34
	v_mov_b32_e32 v146, v34
	v_mov_b32_e32 v147, v34
	v_mov_b32_e32 v148, v34
	v_mov_b32_e32 v149, v34
	v_mov_b32_e32 v150, v34
	v_mov_b32_e32 v151, v34
	v_mov_b32_e32 v152, v34
	v_mov_b32_e32 v153, v34
	v_mov_b32_e32 v102, v34
	v_mov_b32_e32 v103, v34
	v_mov_b32_e32 v104, v34
	v_mov_b32_e32 v105, v34
	v_mov_b32_e32 v110, v34
	v_mov_b32_e32 v111, v34
	v_mov_b32_e32 v112, v34
	v_mov_b32_e32 v113, v34
	v_mov_b32_e32 v118, v34
	v_mov_b32_e32 v119, v34
	v_mov_b32_e32 v120, v34
	v_mov_b32_e32 v121, v34
	v_mov_b32_e32 v126, v34
	v_mov_b32_e32 v127, v34
	v_mov_b32_e32 v128, v34
	v_mov_b32_e32 v129, v34
	v_mov_b32_e32 v134, v34
	v_mov_b32_e32 v135, v34
	v_mov_b32_e32 v136, v34
	v_mov_b32_e32 v137, v34
	v_mov_b32_e32 v142, v34
	v_mov_b32_e32 v143, v34
	v_mov_b32_e32 v144, v34
	v_mov_b32_e32 v145, v34
	v_mov_b32_e32 v154, v34
	v_mov_b32_e32 v155, v34
	v_mov_b32_e32 v156, v34
	v_mov_b32_e32 v157, v34
	v_mov_b32_e32 v158, v34
	v_mov_b32_e32 v159, v34
	v_mov_b32_e32 v160, v34
	v_mov_b32_e32 v161, v34

;     __device__ __forceinline__ void operator()(const f32x4 (&acc)[2][2][4][2], const Unit& u, int wr, int wc, int fr, int fq) const {
;         const int e = u.pn >> 4, pnl = u.pn & 15; const int row0 = u.pm * BM + wr * 64 + fr; const int col0 = pnl * HALF + wc * 32 + 8 * fq;
;         f32x4 bgv[2], buv[2];
; #pragma unroll
;         for (int n = 0; n < 2; ++n) { bgv[n] = *(const f32x4*)(bg + (size_t)e * 2048 + col0 + 4 * n); buv[n] = *(const f32x4*)(bu + (size_t)e * 2048 + col0 + 4 * n); }
; #pragma unroll
;         for (int ai = 0; ai < 2; ++ai)
; #pragma unroll
;             for (int m = 0; m < 4; ++m) { unsigned char* rowp = Y + (size_t)(row0 + ai * HALF + m * 16) * 2048 + col0; f32x4 y[2];
; #pragma unroll
;                 for (int n = 0; n < 2; ++n) { const f32x4 g4 = acc[ai][0][m][n] * wscale + bgv[n], u4 = acc[ai][1][m][n] * wscale + buv[n];
;                     f32x4 gc, uc, ex;
; #pragma unroll
;                     for (int i = 0; i < 4; ++i) { gc[i] = fminf(g4[i], 7.0f); uc[i] = __builtin_amdgcn_fmed3f(u4[i], -7.0f, 7.0f); }
;                     const f32x4 t = gc * (-1.702f * 1.4426950408889634f);
; #pragma unroll
;                     for (int i = 0; i < 4; ++i) ex[i] = __builtin_amdgcn_rcpf(1.0f + __builtin_amdgcn_exp2f(t[i]));
;                     y[n] = (uc + 1.0f) * (gc * ex); }
;                 int w0 = __builtin_amdgcn_cvt_pk_fp8_f32(y[0][0], y[0][1], 0, false); w0 = __builtin_amdgcn_cvt_pk_fp8_f32(y[0][2], y[0][3], w0, true);
;                 int w1 = __builtin_amdgcn_cvt_pk_fp8_f32(y[1][0], y[1][1], 0, false); w1 = __builtin_amdgcn_cvt_pk_fp8_f32(y[1][2], y[1][3], w1, true);
;                 typedef int v2i_t __attribute__((ext_vector_type(2))); *(v2i_t*)rowp = (v2i_t){w0, w1}; }
.LBB0_999:
	s_ashr_i32 s48, s46, 4
	s_lshl_b32 s43, s46, 7
	s_ashr_i32 s49, s48, 31
	s_and_b32 s43, s43, 0x780
	s_lshl_b64 s[48:49], s[48:49], 13
	v_or_b32_e32 v162, s43, v195
	s_add_u32 s50, s16, s48
	s_addc_u32 s51, s17, s49
	v_lshlrev_b32_e32 v2, 2, v162
	v_mov_b64_e32 v[14:15], v[240:241]
	v_mov_b64_e32 v[16:17], v[242:243]
	v_mov_b64_e32 v[6:7], v[248:249]
	v_mov_b64_e32 v[8:9], v[250:251]
	s_add_u32 s48, s20, s48
	s_addc_u32 s49, s21, s49
	v_mov_b64_e32 v[10:11], v[252:253]
	v_mov_b64_e32 v[12:13], v[254:255]
	v_mov_b64_e32 v[2:3], v[244:245]
	v_mov_b32_e32 v4, v247
	v_mov_b32_e32 v5, v190
	v_lshl_add_u32 v20, s62, 8, v171
	v_ashrrev_i32_e32 v21, 31, v20
	v_lshlrev_b64 v[18:19], 11, v[20:21]
	v_mov_b32_e32 v22, v163
	v_mov_b32_e32 v23, v163
	v_lshl_add_u64 v[18:19], s[22:23], 0, v[18:19]
	v_lshl_add_u64 v[18:19], v[18:19], 0, v[162:163]
	v_or_b32_e32 v24, 16, v20
	v_ashrrev_i32_e32 v25, 31, v24
	v_fmamk_f32 v21, v158, 0x3c800000, v14
	v_fmamk_f32 v27, v159, 0x3c800000, v15
	v_fmamk_f32 v30, v154, 0x3c800000, v6
	v_fmamk_f32 v31, v155, 0x3c800000, v7
	v_fmamk_f32 v28, v160, 0x3c800000, v16
	v_fmamk_f32 v32, v156, 0x3c800000, v8
	v_min_f32_e32 v26, 0x40e00000, v21
	v_min_f32_e32 v27, 0x40e00000, v27
	v_min_f32_e32 v30, 0x40e00000, v30
	v_min_f32_e32 v31, 0x40e00000, v31
	v_fmamk_f32 v29, v161, 0x3c800000, v17
	v_fmamk_f32 v33, v157, 0x3c800000, v9
	v_min_f32_e32 v28, 0x40e00000, v28
	v_min_f32_e32 v32, 0x40e00000, v32
	v_fmamk_f32 v21, v150, 0x3c800000, v10
	v_fmamk_f32 v150, v151, 0x3c800000, v11
	v_fmamk_f32 v151, v152, 0x3c800000, v12
	v_fmamk_f32 v152, v153, 0x3c800000, v13
	v_mul_f32_e32 v153, 0xc01d265f, v26
	v_mul_f32_e32 v154, 0xc01d265f, v27
	v_fmamk_f32 v157, v146, 0x3c800000, v2
	v_fmamk_f32 v158, v147, 0x3c800000, v3
	v_mul_f32_e32 v161, 0xc01d265f, v30
	v_mul_f32_e32 v168, 0xc01d265f, v31
	v_mul_f32_e32 v155, 0xc01d265f, v28
	v_fmamk_f32 v159, v148, 0x3c800000, v4
	v_mul_f32_e32 v169, 0xc01d265f, v32
	v_med3_f32 v146, v21, s57, v200
	v_med3_f32 v147, v150, s57, v200
	v_med3_f32 v148, v151, s57, v200
	v_exp_f32_e32 v21, v153
	v_exp_f32_e32 v154, v154
	v_med3_f32 v150, v157, s57, v200
	v_med3_f32 v151, v158, s57, v200
	v_exp_f32_e32 v157, v161
	v_exp_f32_e32 v158, v168
	v_fmamk_f32 v160, v149, 0x3c800000, v5
	v_med3_f32 v149, v152, s57, v200
	v_exp_f32_e32 v155, v155
	v_med3_f32 v152, v159, s57, v200
	v_exp_f32_e32 v159, v169
	v_min_f32_e32 v29, 0x40e00000, v29
	v_min_f32_e32 v33, 0x40e00000, v33
	v_mul_f32_e32 v156, 0xc01d265f, v29
	v_mul_f32_e32 v170, 0xc01d265f, v33
	v_exp_f32_e32 v156, v156
	v_med3_f32 v153, v160, s57, v200
	v_exp_f32_e32 v160, v170
	v_add_f32_e32 v21, 1.0, v21
	v_add_f32_e32 v161, 1.0, v154
	v_add_f32_e32 v170, 1.0, v157
	v_add_f32_e32 v172, 1.0, v158
	v_add_f32_e32 v168, 1.0, v155
	v_add_f32_e32 v173, 1.0, v159
	v_rcp_f32_e32 v154, v21
	v_rcp_f32_e32 v155, v161
	v_rcp_f32_e32 v158, v170
	v_rcp_f32_e32 v159, v172
	v_add_f32_e32 v169, 1.0, v156
	v_add_f32_e32 v174, 1.0, v160
	v_pk_add_f32 v[146:147], v[146:147], 1.0 op_sel_hi:[1,0]
	v_pk_add_f32 v[150:151], v[150:151], 1.0 op_sel_hi:[1,0]
	v_rcp_f32_e32 v156, v168
	v_rcp_f32_e32 v157, v169
	v_rcp_f32_e32 v160, v173
	v_rcp_f32_e32 v161, v174
	v_pk_mul_f32 v[26:27], v[26:27], v[154:155]
	v_pk_mul_f32 v[30:31], v[30:31], v[158:159]
	v_pk_mul_f32 v[26:27], v[146:147], v[26:27]
	v_pk_mul_f32 v[30:31], v[150:151], v[30:31]
	v_cvt_pk_fp8_f32 v22, v26, v27
	v_cvt_pk_fp8_f32 v23, v30, v31
	v_pk_add_f32 v[148:149], v[148:149], 1.0 op_sel_hi:[1,0]
	v_pk_add_f32 v[152:153], v[152:153], 1.0 op_sel_hi:[1,0]
	v_pk_mul_f32 v[28:29], v[28:29], v[156:157]
	v_pk_mul_f32 v[32:33], v[32:33], v[160:161]
	v_pk_mul_f32 v[26:27], v[148:149], v[28:29]
	v_pk_mul_f32 v[28:29], v[152:153], v[32:33]
	v_cvt_pk_fp8_f32 v22, v26, v27 op_sel:[0,0,1]
	v_cvt_pk_fp8_f32 v23, v28, v29 op_sel:[0,0,1]
	v_fmamk_f32 v21, v142, 0x3c800000, v14
	v_min_f32_e32 v26, 0x40e00000, v21
	v_fmamk_f32 v21, v138, 0x3c800000, v10
	global_store_dwordx2 v[18:19], v[22:23], off
	v_med3_f32 v22, v21, s57, v200
	v_fmamk_f32 v21, v143, 0x3c800000, v15
	v_min_f32_e32 v27, 0x40e00000, v21
	v_fmamk_f32 v21, v139, 0x3c800000, v11
	v_mul_f32_e32 v31, 0xc01d265f, v26
	v_med3_f32 v23, v21, s57, v200
	v_fmamk_f32 v21, v144, 0x3c800000, v16
	v_exp_f32_e32 v32, v31
	v_mul_f32_e32 v31, 0xc01d265f, v27
	v_min_f32_e32 v28, 0x40e00000, v21
	v_fmamk_f32 v21, v140, 0x3c800000, v12
	v_exp_f32_e32 v33, v31
	v_med3_f32 v30, v21, s57, v200
	v_fmamk_f32 v21, v145, 0x3c800000, v17
	v_min_f32_e32 v29, 0x40e00000, v21
	v_fmamk_f32 v21, v141, 0x3c800000, v13
	v_med3_f32 v31, v21, s57, v200
	v_add_f32_e32 v21, 1.0, v32
	v_rcp_f32_e32 v32, v21
	v_add_f32_e32 v21, 1.0, v33
	v_mul_f32_e32 v33, 0xc01d265f, v28
	v_exp_f32_e32 v138, v33
	v_mul_f32_e32 v33, 0xc01d265f, v29
	v_exp_f32_e32 v139, v33
	v_rcp_f32_e32 v33, v21
	v_add_f32_e32 v21, 1.0, v138
	v_rcp_f32_e32 v138, v21
	v_add_f32_e32 v21, 1.0, v139
	v_rcp_f32_e32 v139, v21
	v_pk_add_f32 v[22:23], v[22:23], 1.0 op_sel_hi:[1,0]
	v_pk_mul_f32 v[26:27], v[26:27], v[32:33]
	v_fmamk_f32 v21, v134, 0x3c800000, v6
	v_pk_add_f32 v[30:31], v[30:31], 1.0 op_sel_hi:[1,0]
	v_pk_mul_f32 v[28:29], v[28:29], v[138:139]
	v_pk_mul_f32 v[22:23], v[22:23], v[26:27]
	v_min_f32_e32 v26, 0x40e00000, v21
	v_fmamk_f32 v21, v130, 0x3c800000, v2
	v_pk_mul_f32 v[28:29], v[30:31], v[28:29]
	v_med3_f32 v30, v21, s57, v200
	v_fmamk_f32 v21, v135, 0x3c800000, v7
	v_min_f32_e32 v27, 0x40e00000, v21
	v_fmamk_f32 v21, v131, 0x3c800000, v3
	v_med3_f32 v31, v21, s57, v200
	v_fmamk_f32 v21, v136, 0x3c800000, v8
	v_min_f32_e32 v32, 0x40e00000, v21
	v_fmamk_f32 v21, v132, 0x3c800000, v4
	v_mul_f32_e32 v131, 0xc01d265f, v26
;     __device__ __forceinline__ void operator()(const f32x4 (&acc)[2][2][4][2], const Unit& u, int wr, int wc, int fr, int fq) const {
;     ...
;             for (int m = 0; m < 4; ++m) { unsigned char* rowp = Y + (size_t)(row0 + ai * HALF + m * 16) * 2048 + col0; f32x4 y[2];
; #pragma unroll
;                 for (int n = 0; n < 2; ++n) { const f32x4 g4 = acc[ai][0][m][n] * wscale + bgv[n], u4 = acc[ai][1][m][n] * wscale + buv[n];
;                     f32x4 gc, uc, ex;
; #pragma unroll
;                     for (int i = 0; i < 4; ++i) { gc[i] = fminf(g4[i], 7.0f); uc[i] = __builtin_amdgcn_fmed3f(u4[i], -7.0f, 7.0f); }
;                     const f32x4 t = gc * (-1.702f * 1.4426950408889634f);
; #pragma unroll
;                     for (int i = 0; i < 4; ++i) ex[i] = __builtin_amdgcn_rcpf(1.0f + __builtin_amdgcn_exp2f(t[i]));
;                     y[n] = (uc + 1.0f) * (gc * ex); }
;                 int w0 = __builtin_amdgcn_cvt_pk_fp8_f32(y[0][0], y[0][1], 0, false); w0 = __builtin_amdgcn_cvt_pk_fp8_f32(y[0][2], y[0][3], w0, true);
;                 int w1 = __builtin_amdgcn_cvt_pk_fp8_f32(y[1][0], y[1][1], 0, false); w1 = __builtin_amdgcn_cvt_pk_fp8_f32(y[1][2], y[1][3], w1, true);
;                 typedef int v2i_t __attribute__((ext_vector_type(2))); *(v2i_t*)rowp = (v2i_t){w0, w1}; }
	v_med3_f32 v130, v21, s57, v200
	v_fmamk_f32 v21, v137, 0x3c800000, v9
	v_exp_f32_e32 v132, v131
	v_mul_f32_e32 v131, 0xc01d265f, v27
	v_min_f32_e32 v33, 0x40e00000, v21
	v_fmamk_f32 v21, v133, 0x3c800000, v5
	v_exp_f32_e32 v133, v131
	v_med3_f32 v131, v21, s57, v200
	v_add_f32_e32 v21, 1.0, v132
	v_rcp_f32_e32 v132, v21
	v_add_f32_e32 v21, 1.0, v133
	v_mul_f32_e32 v133, 0xc01d265f, v32
	v_exp_f32_e32 v134, v133
	v_mul_f32_e32 v133, 0xc01d265f, v33
	v_exp_f32_e32 v135, v133
	v_rcp_f32_e32 v133, v21
	v_add_f32_e32 v21, 1.0, v134
	v_rcp_f32_e32 v134, v21
	v_add_f32_e32 v21, 1.0, v135
	v_rcp_f32_e32 v135, v21
	v_pk_add_f32 v[30:31], v[30:31], 1.0 op_sel_hi:[1,0]
	v_pk_mul_f32 v[26:27], v[26:27], v[132:133]
	v_pk_add_f32 v[130:131], v[130:131], 1.0 op_sel_hi:[1,0]
	v_pk_mul_f32 v[26:27], v[30:31], v[26:27]
	v_mov_b32_e32 v30, v163
	v_mov_b32_e32 v31, v163
	v_cvt_pk_fp8_f32 v30, v22, v23
	v_cvt_pk_fp8_f32 v31, v26, v27
	v_pk_mul_f32 v[22:23], v[32:33], v[134:135]
	v_fmamk_f32 v21, v126, 0x3c800000, v14
	v_pk_mul_f32 v[22:23], v[130:131], v[22:23]
	v_cvt_pk_fp8_f32 v30, v28, v29 op_sel:[0,0,1]
	v_cvt_pk_fp8_f32 v31, v22, v23 op_sel:[0,0,1]
	v_lshlrev_b64 v[22:23], 11, v[24:25]
	v_lshl_add_u64 v[22:23], s[22:23], 0, v[22:23]
	v_min_f32_e32 v24, 0x40e00000, v21
	v_fmamk_f32 v21, v122, 0x3c800000, v10
	v_lshl_add_u64 v[22:23], v[22:23], 0, v[162:163]
	v_med3_f32 v26, v21, s57, v200
	v_fmamk_f32 v21, v127, 0x3c800000, v15
	global_store_dwordx2 v[22:23], v[30:31], off
	v_min_f32_e32 v25, 0x40e00000, v21
	v_fmamk_f32 v21, v123, 0x3c800000, v11
	v_mul_f32_e32 v31, 0xc01d265f, v24
	v_med3_f32 v27, v21, s57, v200
	v_fmamk_f32 v21, v128, 0x3c800000, v16
	v_exp_f32_e32 v32, v31
	v_mul_f32_e32 v31, 0xc01d265f, v25
	v_min_f32_e32 v28, 0x40e00000, v21
	v_fmamk_f32 v21, v124, 0x3c800000, v12
	v_exp_f32_e32 v33, v31
	v_med3_f32 v30, v21, s57, v200
	v_fmamk_f32 v21, v129, 0x3c800000, v17
	v_min_f32_e32 v29, 0x40e00000, v21
	v_fmamk_f32 v21, v125, 0x3c800000, v13
	v_med3_f32 v31, v21, s57, v200
	v_add_f32_e32 v21, 1.0, v32
	v_rcp_f32_e32 v32, v21
	v_add_f32_e32 v21, 1.0, v33
	v_mul_f32_e32 v33, 0xc01d265f, v28
	v_exp_f32_e32 v122, v33
	v_mul_f32_e32 v33, 0xc01d265f, v29
	v_exp_f32_e32 v123, v33
	v_rcp_f32_e32 v33, v21
	v_add_f32_e32 v21, 1.0, v122
	v_rcp_f32_e32 v122, v21
	v_add_f32_e32 v21, 1.0, v123
	v_rcp_f32_e32 v123, v21
	v_pk_add_f32 v[26:27], v[26:27], 1.0 op_sel_hi:[1,0]
	v_pk_mul_f32 v[24:25], v[24:25], v[32:33]
	v_fmamk_f32 v21, v118, 0x3c800000, v6
	v_pk_add_f32 v[30:31], v[30:31], 1.0 op_sel_hi:[1,0]
	v_pk_mul_f32 v[28:29], v[28:29], v[122:123]
	v_pk_mul_f32 v[24:25], v[26:27], v[24:25]
	v_min_f32_e32 v26, 0x40e00000, v21
	v_fmamk_f32 v21, v114, 0x3c800000, v2
	v_pk_mul_f32 v[28:29], v[30:31], v[28:29]
	v_med3_f32 v30, v21, s57, v200
	v_fmamk_f32 v21, v119, 0x3c800000, v7
	v_min_f32_e32 v27, 0x40e00000, v21
	v_fmamk_f32 v21, v115, 0x3c800000, v3
	v_med3_f32 v31, v21, s57, v200
	v_fmamk_f32 v21, v120, 0x3c800000, v8
	v_min_f32_e32 v32, 0x40e00000, v21
	v_fmamk_f32 v21, v116, 0x3c800000, v4
	v_mul_f32_e32 v115, 0xc01d265f, v26
	v_med3_f32 v114, v21, s57, v200
	v_fmamk_f32 v21, v121, 0x3c800000, v9
	v_exp_f32_e32 v116, v115
	v_mul_f32_e32 v115, 0xc01d265f, v27
	v_min_f32_e32 v33, 0x40e00000, v21
	v_fmamk_f32 v21, v117, 0x3c800000, v5
	v_exp_f32_e32 v117, v115
	v_med3_f32 v115, v21, s57, v200
	v_add_f32_e32 v21, 1.0, v116
	v_rcp_f32_e32 v116, v21
	v_add_f32_e32 v21, 1.0, v117
	v_mul_f32_e32 v117, 0xc01d265f, v32
	v_exp_f32_e32 v118, v117
	v_mul_f32_e32 v117, 0xc01d265f, v33
	v_exp_f32_e32 v119, v117
	v_rcp_f32_e32 v117, v21
	v_add_f32_e32 v21, 1.0, v118
	v_rcp_f32_e32 v118, v21
	v_add_f32_e32 v21, 1.0, v119
	v_rcp_f32_e32 v119, v21
	v_pk_add_f32 v[30:31], v[30:31], 1.0 op_sel_hi:[1,0]
	v_pk_mul_f32 v[26:27], v[26:27], v[116:117]
	v_pk_add_f32 v[114:115], v[114:115], 1.0 op_sel_hi:[1,0]
	v_pk_mul_f32 v[26:27], v[30:31], v[26:27]
	v_mov_b32_e32 v30, v163
	v_mov_b32_e32 v31, v163
	v_cvt_pk_fp8_f32 v30, v24, v25
	v_cvt_pk_fp8_f32 v31, v26, v27
	v_pk_mul_f32 v[24:25], v[32:33], v[118:119]
	v_or_b32_e32 v22, 32, v20
	v_pk_mul_f32 v[24:25], v[114:115], v[24:25]
	v_ashrrev_i32_e32 v23, 31, v22
	v_cvt_pk_fp8_f32 v30, v28, v29 op_sel:[0,0,1]
	v_cvt_pk_fp8_f32 v31, v24, v25 op_sel:[0,0,1]
	v_lshlrev_b64 v[22:23], 11, v[22:23]
	v_lshl_add_u64 v[22:23], s[22:23], 0, v[22:23]
	v_lshl_add_u64 v[22:23], v[22:23], 0, v[162:163]
	global_store_dwordx2 v[22:23], v[30:31], off
	v_fmamk_f32 v23, v106, 0x3c800000, v10
	v_fmamk_f32 v22, v110, 0x3c800000, v14
	v_med3_f32 v24, v23, s57, v200
	v_fmamk_f32 v23, v111, 0x3c800000, v15
	v_fmamk_f32 v27, v108, 0x3c800000, v12
	v_min_f32_e32 v22, 0x40e00000, v22
	v_min_f32_e32 v23, 0x40e00000, v23
	v_fmamk_f32 v26, v112, 0x3c800000, v16
	v_med3_f32 v28, v27, s57, v200
	v_fmamk_f32 v27, v113, 0x3c800000, v17
	v_min_f32_e32 v26, 0x40e00000, v26
	v_min_f32_e32 v27, 0x40e00000, v27
	v_mul_f32_e32 v30, 0xc01d265f, v22
	v_mul_f32_e32 v31, 0xc01d265f, v23
	v_exp_f32_e32 v30, v30
	v_exp_f32_e32 v31, v31
	v_mul_f32_e32 v32, 0xc01d265f, v26
	v_mul_f32_e32 v33, 0xc01d265f, v27
	v_exp_f32_e32 v32, v32
	v_exp_f32_e32 v33, v33
	v_add_f32_e32 v30, 1.0, v30
	v_add_f32_e32 v31, 1.0, v31
	v_rcp_f32_e32 v30, v30
	v_rcp_f32_e32 v31, v31
	v_add_f32_e32 v32, 1.0, v32
	v_add_f32_e32 v33, 1.0, v33
	v_rcp_f32_e32 v32, v32
	v_rcp_f32_e32 v33, v33
	v_fmamk_f32 v25, v107, 0x3c800000, v11
	v_med3_f32 v25, v25, s57, v200
	v_fmamk_f32 v29, v109, 0x3c800000, v13
	v_med3_f32 v29, v29, s57, v200
	v_pk_add_f32 v[24:25], v[24:25], 1.0 op_sel_hi:[1,0]
	v_pk_mul_f32 v[22:23], v[22:23], v[30:31]
	v_pk_add_f32 v[28:29], v[28:29], 1.0 op_sel_hi:[1,0]
;     __device__ __forceinline__ void operator()(const f32x4 (&acc)[2][2][4][2], const Unit& u, int wr, int wc, int fr, int fq) const {
;     ...
;             for (int m = 0; m < 4; ++m) { unsigned char* rowp = Y + (size_t)(row0 + ai * HALF + m * 16) * 2048 + col0; f32x4 y[2];
; #pragma unroll
;                 for (int n = 0; n < 2; ++n) { const f32x4 g4 = acc[ai][0][m][n] * wscale + bgv[n], u4 = acc[ai][1][m][n] * wscale + buv[n];
;                     f32x4 gc, uc, ex;
; #pragma unroll
;                     for (int i = 0; i < 4; ++i) { gc[i] = fminf(g4[i], 7.0f); uc[i] = __builtin_amdgcn_fmed3f(u4[i], -7.0f, 7.0f); }
;                     const f32x4 t = gc * (-1.702f * 1.4426950408889634f);
; #pragma unroll
;                     for (int i = 0; i < 4; ++i) ex[i] = __builtin_amdgcn_rcpf(1.0f + __builtin_amdgcn_exp2f(t[i]));
;                     y[n] = (uc + 1.0f) * (gc * ex); }
;                 int w0 = __builtin_amdgcn_cvt_pk_fp8_f32(y[0][0], y[0][1], 0, false); w0 = __builtin_amdgcn_cvt_pk_fp8_f32(y[0][2], y[0][3], w0, true);
;                 int w1 = __builtin_amdgcn_cvt_pk_fp8_f32(y[1][0], y[1][1], 0, false); w1 = __builtin_amdgcn_cvt_pk_fp8_f32(y[1][2], y[1][3], w1, true);
;                 typedef int v2i_t __attribute__((ext_vector_type(2))); *(v2i_t*)rowp = (v2i_t){w0, w1}; }
	v_pk_mul_f32 v[26:27], v[26:27], v[32:33]
	v_pk_mul_f32 v[22:23], v[24:25], v[22:23]
	v_fmamk_f32 v25, v98, 0x3c800000, v2
	v_pk_mul_f32 v[26:27], v[28:29], v[26:27]
	v_fmamk_f32 v24, v102, 0x3c800000, v6
	v_med3_f32 v28, v25, s57, v200
	v_fmamk_f32 v25, v103, 0x3c800000, v7
	v_min_f32_e32 v24, 0x40e00000, v24
	v_min_f32_e32 v25, 0x40e00000, v25
	v_fmamk_f32 v29, v99, 0x3c800000, v3
	v_mul_f32_e32 v98, 0xc01d265f, v24
	v_mul_f32_e32 v99, 0xc01d265f, v25
	v_fmamk_f32 v31, v100, 0x3c800000, v4
	v_exp_f32_e32 v98, v98
	v_exp_f32_e32 v99, v99
	v_fmamk_f32 v30, v104, 0x3c800000, v8
	v_med3_f32 v32, v31, s57, v200
	v_fmamk_f32 v31, v105, 0x3c800000, v9
	v_min_f32_e32 v30, 0x40e00000, v30
	v_min_f32_e32 v31, 0x40e00000, v31
	v_fmamk_f32 v33, v101, 0x3c800000, v5
	v_mul_f32_e32 v100, 0xc01d265f, v30
	v_mul_f32_e32 v101, 0xc01d265f, v31
	v_add_f32_e32 v98, 1.0, v98
	v_add_f32_e32 v99, 1.0, v99
	v_exp_f32_e32 v100, v100
	v_exp_f32_e32 v101, v101
	v_rcp_f32_e32 v98, v98
	v_rcp_f32_e32 v99, v99
	v_med3_f32 v29, v29, s57, v200
	v_add_f32_e32 v100, 1.0, v100
	v_add_f32_e32 v101, 1.0, v101
	v_rcp_f32_e32 v100, v100
	v_rcp_f32_e32 v101, v101
	v_pk_add_f32 v[28:29], v[28:29], 1.0 op_sel_hi:[1,0]
	v_pk_mul_f32 v[24:25], v[24:25], v[98:99]
	v_med3_f32 v33, v33, s57, v200
	v_pk_mul_f32 v[24:25], v[28:29], v[24:25]
	v_mov_b32_e32 v28, v163
	v_mov_b32_e32 v29, v163
	v_cvt_pk_fp8_f32 v28, v22, v23
	v_cvt_pk_fp8_f32 v29, v24, v25
	v_pk_add_f32 v[32:33], v[32:33], 1.0 op_sel_hi:[1,0]
	v_pk_mul_f32 v[22:23], v[30:31], v[100:101]
	v_or_b32_e32 v20, 48, v20
	v_pk_mul_f32 v[22:23], v[32:33], v[22:23]
	v_ashrrev_i32_e32 v21, 31, v20
	v_cvt_pk_fp8_f32 v28, v26, v27 op_sel:[0,0,1]
	v_cvt_pk_fp8_f32 v29, v22, v23 op_sel:[0,0,1]
	v_lshlrev_b64 v[20:21], 11, v[20:21]
	v_lshl_add_u64 v[20:21], s[22:23], 0, v[20:21]
	v_lshl_add_u64 v[20:21], v[20:21], 0, v[162:163]
	global_store_dwordx2 v[20:21], v[28:29], off
	v_fmamk_f32 v21, v90, 0x3c800000, v10
	v_fmamk_f32 v20, v94, 0x3c800000, v14
	v_med3_f32 v22, v21, s57, v200
	v_fmamk_f32 v21, v95, 0x3c800000, v15
	v_fmamk_f32 v25, v92, 0x3c800000, v12
	v_min_f32_e32 v20, 0x40e00000, v20
	v_min_f32_e32 v21, 0x40e00000, v21
	v_fmamk_f32 v24, v96, 0x3c800000, v16
	v_med3_f32 v26, v25, s57, v200
	v_fmamk_f32 v25, v97, 0x3c800000, v17
	v_min_f32_e32 v24, 0x40e00000, v24
	v_min_f32_e32 v25, 0x40e00000, v25
	v_mul_f32_e32 v28, 0xc01d265f, v20
	v_mul_f32_e32 v29, 0xc01d265f, v21
	v_exp_f32_e32 v28, v28
	v_exp_f32_e32 v29, v29
	v_mul_f32_e32 v30, 0xc01d265f, v24
	v_mul_f32_e32 v31, 0xc01d265f, v25
	v_exp_f32_e32 v30, v30
	v_exp_f32_e32 v31, v31
	v_add_f32_e32 v28, 1.0, v28
	v_add_f32_e32 v29, 1.0, v29
	v_rcp_f32_e32 v28, v28
	v_rcp_f32_e32 v29, v29
	v_add_f32_e32 v30, 1.0, v30
	v_add_f32_e32 v31, 1.0, v31
	v_rcp_f32_e32 v30, v30
	v_rcp_f32_e32 v31, v31
	v_fmamk_f32 v23, v91, 0x3c800000, v11
	v_med3_f32 v23, v23, s57, v200
	v_fmamk_f32 v27, v93, 0x3c800000, v13
	v_med3_f32 v27, v27, s57, v200
	v_pk_add_f32 v[22:23], v[22:23], 1.0 op_sel_hi:[1,0]
	v_pk_mul_f32 v[20:21], v[20:21], v[28:29]
	v_pk_add_f32 v[26:27], v[26:27], 1.0 op_sel_hi:[1,0]
	v_pk_mul_f32 v[24:25], v[24:25], v[30:31]
	v_pk_mul_f32 v[20:21], v[22:23], v[20:21]
	v_fmamk_f32 v23, v82, 0x3c800000, v2
	v_pk_mul_f32 v[24:25], v[26:27], v[24:25]
	v_fmamk_f32 v22, v86, 0x3c800000, v6
	v_med3_f32 v26, v23, s57, v200
	v_fmamk_f32 v23, v87, 0x3c800000, v7
	v_min_f32_e32 v22, 0x40e00000, v22
	v_min_f32_e32 v23, 0x40e00000, v23
	v_mul_f32_e32 v32, 0xc01d265f, v22
	v_mul_f32_e32 v33, 0xc01d265f, v23
	v_fmamk_f32 v29, v84, 0x3c800000, v4
	v_exp_f32_e32 v32, v32
	v_exp_f32_e32 v33, v33
	v_fmamk_f32 v28, v88, 0x3c800000, v8
	v_med3_f32 v30, v29, s57, v200
	v_fmamk_f32 v29, v89, 0x3c800000, v9
	v_min_f32_e32 v28, 0x40e00000, v28
	v_min_f32_e32 v29, 0x40e00000, v29
	v_fmamk_f32 v27, v83, 0x3c800000, v3
	v_mul_f32_e32 v82, 0xc01d265f, v28
	v_mul_f32_e32 v83, 0xc01d265f, v29
	v_add_f32_e32 v32, 1.0, v32
	v_add_f32_e32 v33, 1.0, v33
	v_exp_f32_e32 v82, v82
	v_exp_f32_e32 v83, v83
	v_rcp_f32_e32 v32, v32
	v_rcp_f32_e32 v33, v33
	v_med3_f32 v27, v27, s57, v200
	v_add_f32_e32 v82, 1.0, v82
	v_add_f32_e32 v83, 1.0, v83
	v_rcp_f32_e32 v82, v82
	v_rcp_f32_e32 v83, v83
	v_pk_add_f32 v[26:27], v[26:27], 1.0 op_sel_hi:[1,0]
	v_pk_mul_f32 v[22:23], v[22:23], v[32:33]
	v_fmamk_f32 v31, v85, 0x3c800000, v5
	v_pk_mul_f32 v[22:23], v[26:27], v[22:23]
	v_mov_b32_e32 v26, v163
	v_mov_b32_e32 v27, v163
	v_cvt_pk_fp8_f32 v26, v20, v21
	v_cvt_pk_fp8_f32 v27, v22, v23
	v_med3_f32 v31, v31, s57, v200
	v_pk_add_f32 v[30:31], v[30:31], 1.0 op_sel_hi:[1,0]
	v_pk_mul_f32 v[20:21], v[28:29], v[82:83]
	v_cvt_pk_fp8_f32 v26, v24, v25 op_sel:[0,0,1]
	v_pk_mul_f32 v[20:21], v[30:31], v[20:21]
	v_fmamk_f32 v25, v76, 0x3c800000, v12
	v_cvt_pk_fp8_f32 v27, v20, v21 op_sel:[0,0,1]
	v_add_co_u32_e32 v20, vcc, s58, v18
	v_fmamk_f32 v24, v80, 0x3c800000, v16
	s_nop 0
	v_addc_co_u32_e32 v21, vcc, 0, v19, vcc
	global_store_dwordx2 v[20:21], v[26:27], off
	v_fmamk_f32 v21, v74, 0x3c800000, v10
	v_fmamk_f32 v20, v78, 0x3c800000, v14
	v_med3_f32 v22, v21, s57, v200
	v_fmamk_f32 v21, v79, 0x3c800000, v15
	v_min_f32_e32 v20, 0x40e00000, v20
	v_min_f32_e32 v21, 0x40e00000, v21
	v_med3_f32 v26, v25, s57, v200
	v_fmamk_f32 v25, v81, 0x3c800000, v17
	v_min_f32_e32 v24, 0x40e00000, v24
	v_min_f32_e32 v25, 0x40e00000, v25
	v_mul_f32_e32 v28, 0xc01d265f, v20
	v_mul_f32_e32 v29, 0xc01d265f, v21
	v_exp_f32_e32 v28, v28
	v_exp_f32_e32 v29, v29
	v_mul_f32_e32 v30, 0xc01d265f, v24
	v_mul_f32_e32 v31, 0xc01d265f, v25
	v_exp_f32_e32 v30, v30
	v_exp_f32_e32 v31, v31
	v_add_f32_e32 v28, 1.0, v28
	v_add_f32_e32 v29, 1.0, v29
	v_rcp_f32_e32 v28, v28
;     __device__ __forceinline__ void operator()(const f32x4 (&acc)[2][2][4][2], const Unit& u, int wr, int wc, int fr, int fq) const {
;     ...
;             for (int m = 0; m < 4; ++m) { unsigned char* rowp = Y + (size_t)(row0 + ai * HALF + m * 16) * 2048 + col0; f32x4 y[2];
; #pragma unroll
;                 for (int n = 0; n < 2; ++n) { const f32x4 g4 = acc[ai][0][m][n] * wscale + bgv[n], u4 = acc[ai][1][m][n] * wscale + buv[n];
;                     f32x4 gc, uc, ex;
; #pragma unroll
;                     for (int i = 0; i < 4; ++i) { gc[i] = fminf(g4[i], 7.0f); uc[i] = __builtin_amdgcn_fmed3f(u4[i], -7.0f, 7.0f); }
;                     const f32x4 t = gc * (-1.702f * 1.4426950408889634f);
; #pragma unroll
;                     for (int i = 0; i < 4; ++i) ex[i] = __builtin_amdgcn_rcpf(1.0f + __builtin_amdgcn_exp2f(t[i]));
;                     y[n] = (uc + 1.0f) * (gc * ex); }
;                 int w0 = __builtin_amdgcn_cvt_pk_fp8_f32(y[0][0], y[0][1], 0, false); w0 = __builtin_amdgcn_cvt_pk_fp8_f32(y[0][2], y[0][3], w0, true);
;                 int w1 = __builtin_amdgcn_cvt_pk_fp8_f32(y[1][0], y[1][1], 0, false); w1 = __builtin_amdgcn_cvt_pk_fp8_f32(y[1][2], y[1][3], w1, true);
;                 typedef int v2i_t __attribute__((ext_vector_type(2))); *(v2i_t*)rowp = (v2i_t){w0, w1}; }
	v_rcp_f32_e32 v29, v29
	v_add_f32_e32 v30, 1.0, v30
	v_add_f32_e32 v31, 1.0, v31
	v_rcp_f32_e32 v30, v30
	v_rcp_f32_e32 v31, v31
	v_fmamk_f32 v23, v75, 0x3c800000, v11
	v_med3_f32 v23, v23, s57, v200
	v_fmamk_f32 v27, v77, 0x3c800000, v13
	v_med3_f32 v27, v27, s57, v200
	v_pk_add_f32 v[22:23], v[22:23], 1.0 op_sel_hi:[1,0]
	v_pk_mul_f32 v[20:21], v[20:21], v[28:29]
	v_pk_add_f32 v[26:27], v[26:27], 1.0 op_sel_hi:[1,0]
	v_pk_mul_f32 v[24:25], v[24:25], v[30:31]
	v_pk_mul_f32 v[20:21], v[22:23], v[20:21]
	v_fmamk_f32 v23, v66, 0x3c800000, v2
	v_pk_mul_f32 v[24:25], v[26:27], v[24:25]
	v_fmamk_f32 v22, v70, 0x3c800000, v6
	v_med3_f32 v26, v23, s57, v200
	v_fmamk_f32 v23, v71, 0x3c800000, v7
	v_min_f32_e32 v22, 0x40e00000, v22
	v_min_f32_e32 v23, 0x40e00000, v23
	v_mul_f32_e32 v32, 0xc01d265f, v22
	v_mul_f32_e32 v33, 0xc01d265f, v23
	v_fmamk_f32 v29, v68, 0x3c800000, v4
	v_exp_f32_e32 v32, v32
	v_exp_f32_e32 v33, v33
	v_fmamk_f32 v28, v72, 0x3c800000, v8
	v_med3_f32 v30, v29, s57, v200
	v_fmamk_f32 v29, v73, 0x3c800000, v9
	v_min_f32_e32 v28, 0x40e00000, v28
	v_min_f32_e32 v29, 0x40e00000, v29
	v_fmamk_f32 v27, v67, 0x3c800000, v3
	v_mul_f32_e32 v66, 0xc01d265f, v28
	v_mul_f32_e32 v67, 0xc01d265f, v29
	v_add_f32_e32 v32, 1.0, v32
	v_add_f32_e32 v33, 1.0, v33
	v_exp_f32_e32 v66, v66
	v_exp_f32_e32 v67, v67
	v_rcp_f32_e32 v32, v32
	v_rcp_f32_e32 v33, v33
	v_med3_f32 v27, v27, s57, v200
	v_add_f32_e32 v66, 1.0, v66
	v_add_f32_e32 v67, 1.0, v67
	v_rcp_f32_e32 v66, v66
	v_rcp_f32_e32 v67, v67
	v_pk_add_f32 v[26:27], v[26:27], 1.0 op_sel_hi:[1,0]
	v_pk_mul_f32 v[22:23], v[22:23], v[32:33]
	v_fmamk_f32 v31, v69, 0x3c800000, v5
	v_pk_mul_f32 v[22:23], v[26:27], v[22:23]
	v_mov_b32_e32 v26, v163
	v_mov_b32_e32 v27, v163
	v_cvt_pk_fp8_f32 v26, v20, v21
	v_cvt_pk_fp8_f32 v27, v22, v23
	v_med3_f32 v31, v31, s57, v200
	v_pk_add_f32 v[30:31], v[30:31], 1.0 op_sel_hi:[1,0]
	v_pk_mul_f32 v[20:21], v[28:29], v[66:67]
	v_cvt_pk_fp8_f32 v26, v24, v25 op_sel:[0,0,1]
	v_pk_mul_f32 v[20:21], v[30:31], v[20:21]
	v_fmamk_f32 v25, v60, 0x3c800000, v12
	v_cvt_pk_fp8_f32 v27, v20, v21 op_sel:[0,0,1]
	v_add_co_u32_e32 v20, vcc, s59, v18
	v_fmamk_f32 v24, v64, 0x3c800000, v16
	s_nop 0
	v_addc_co_u32_e32 v21, vcc, 0, v19, vcc
	global_store_dwordx2 v[20:21], v[26:27], off
	v_fmamk_f32 v21, v58, 0x3c800000, v10
	v_fmamk_f32 v20, v62, 0x3c800000, v14
	v_med3_f32 v22, v21, s57, v200
	v_fmamk_f32 v21, v63, 0x3c800000, v15
	v_min_f32_e32 v20, 0x40e00000, v20
	v_min_f32_e32 v21, 0x40e00000, v21
	v_med3_f32 v26, v25, s57, v200
	v_fmamk_f32 v25, v65, 0x3c800000, v17
	v_min_f32_e32 v24, 0x40e00000, v24
	v_min_f32_e32 v25, 0x40e00000, v25
	v_mul_f32_e32 v28, 0xc01d265f, v20
	v_mul_f32_e32 v29, 0xc01d265f, v21
	v_exp_f32_e32 v28, v28
	v_exp_f32_e32 v29, v29
	v_mul_f32_e32 v30, 0xc01d265f, v24
	v_mul_f32_e32 v31, 0xc01d265f, v25
	v_exp_f32_e32 v30, v30
	v_exp_f32_e32 v31, v31
	v_add_f32_e32 v28, 1.0, v28
	v_add_f32_e32 v29, 1.0, v29
	v_rcp_f32_e32 v28, v28
	v_rcp_f32_e32 v29, v29
	v_add_f32_e32 v30, 1.0, v30
	v_add_f32_e32 v31, 1.0, v31
	v_rcp_f32_e32 v30, v30
	v_rcp_f32_e32 v31, v31
	v_fmamk_f32 v23, v59, 0x3c800000, v11
	v_med3_f32 v23, v23, s57, v200
	v_fmamk_f32 v27, v61, 0x3c800000, v13
	v_med3_f32 v27, v27, s57, v200
	v_pk_add_f32 v[22:23], v[22:23], 1.0 op_sel_hi:[1,0]
	v_pk_mul_f32 v[20:21], v[20:21], v[28:29]
	v_pk_add_f32 v[26:27], v[26:27], 1.0 op_sel_hi:[1,0]
	v_pk_mul_f32 v[24:25], v[24:25], v[30:31]
	v_pk_mul_f32 v[20:21], v[22:23], v[20:21]
	v_fmamk_f32 v23, v50, 0x3c800000, v2
	v_pk_mul_f32 v[24:25], v[26:27], v[24:25]
	v_fmamk_f32 v22, v54, 0x3c800000, v6
	v_med3_f32 v26, v23, s57, v200
	v_fmamk_f32 v23, v55, 0x3c800000, v7
	v_min_f32_e32 v22, 0x40e00000, v22
	v_min_f32_e32 v23, 0x40e00000, v23
	v_mul_f32_e32 v32, 0xc01d265f, v22
	v_mul_f32_e32 v33, 0xc01d265f, v23
	v_fmamk_f32 v29, v52, 0x3c800000, v4
	v_exp_f32_e32 v32, v32
	v_exp_f32_e32 v33, v33
	v_fmamk_f32 v28, v56, 0x3c800000, v8
	v_med3_f32 v30, v29, s57, v200
	v_fmamk_f32 v29, v57, 0x3c800000, v9
	v_min_f32_e32 v28, 0x40e00000, v28
	v_min_f32_e32 v29, 0x40e00000, v29
	v_fmamk_f32 v27, v51, 0x3c800000, v3
	v_mul_f32_e32 v50, 0xc01d265f, v28
	v_mul_f32_e32 v51, 0xc01d265f, v29
; #define PG8_WAIT_V(n) asm volatile("s_waitcnt vmcnt(" #n ")" ::: "memory")
; #define PG8_BAR __builtin_amdgcn_s_barrier()
; template <class Epi, class Sched, bool ALIGN_EPI = false, bool SP2 = false, bool F8 = false, bool GATHER = false>
; __device__ __forceinline__ void gemm_phase(PG8_LAS unsigned char* lds, const Gemm g, const Sched& S, const Epi& E) {
;     ...
;     PG8_WAIT_V(0);
;     if constexpr (!ALIGN_EPI) { if (wr == 0) PG8_BAR; }
;     PG8_BAR;
;     __device__ __forceinline__ void operator()(const f32x4 (&acc)[2][2][4][2], const Unit& u, int wr, int wc, int fr, int fq) const {
;     ...
;                 for (int n = 0; n < 2; ++n) { const f32x4 g4 = acc[ai][0][m][n] * wscale + bgv[n], u4 = acc[ai][1][m][n] * wscale + buv[n];
;                     f32x4 gc, uc, ex;
; #pragma unroll
;                     for (int i = 0; i < 4; ++i) { gc[i] = fminf(g4[i], 7.0f); uc[i] = __builtin_amdgcn_fmed3f(u4[i], -7.0f, 7.0f); }
;                     const f32x4 t = gc * (-1.702f * 1.4426950408889634f);
; #pragma unroll
;                     for (int i = 0; i < 4; ++i) ex[i] = __builtin_amdgcn_rcpf(1.0f + __builtin_amdgcn_exp2f(t[i]));
;                     y[n] = (uc + 1.0f) * (gc * ex); }
;                 int w0 = __builtin_amdgcn_cvt_pk_fp8_f32(y[0][0], y[0][1], 0, false); w0 = __builtin_amdgcn_cvt_pk_fp8_f32(y[0][2], y[0][3], w0, true);
;                 int w1 = __builtin_amdgcn_cvt_pk_fp8_f32(y[1][0], y[1][1], 0, false); w1 = __builtin_amdgcn_cvt_pk_fp8_f32(y[1][2], y[1][3], w1, true);
;                 typedef int v2i_t __attribute__((ext_vector_type(2))); *(v2i_t*)rowp = (v2i_t){w0, w1}; }
	v_add_f32_e32 v32, 1.0, v32
	v_add_f32_e32 v33, 1.0, v33
	v_exp_f32_e32 v50, v50
	v_exp_f32_e32 v51, v51
	v_rcp_f32_e32 v32, v32
	v_rcp_f32_e32 v33, v33
	v_med3_f32 v27, v27, s57, v200
	v_add_f32_e32 v50, 1.0, v50
	v_add_f32_e32 v51, 1.0, v51
	v_rcp_f32_e32 v50, v50
	v_rcp_f32_e32 v51, v51
	v_pk_add_f32 v[26:27], v[26:27], 1.0 op_sel_hi:[1,0]
	v_pk_mul_f32 v[22:23], v[22:23], v[32:33]
	v_fmamk_f32 v31, v53, 0x3c800000, v5
	v_pk_mul_f32 v[22:23], v[26:27], v[22:23]
	v_mov_b32_e32 v26, v163
	v_mov_b32_e32 v27, v163
	v_cvt_pk_fp8_f32 v26, v20, v21
	v_cvt_pk_fp8_f32 v27, v22, v23
	v_med3_f32 v31, v31, s57, v200
	v_pk_add_f32 v[30:31], v[30:31], 1.0 op_sel_hi:[1,0]
	v_pk_mul_f32 v[20:21], v[28:29], v[50:51]
	v_cvt_pk_fp8_f32 v26, v24, v25 op_sel:[0,0,1]
	v_pk_mul_f32 v[20:21], v[30:31], v[20:21]
	v_fmamk_f32 v14, v46, 0x3c800000, v14
	v_cvt_pk_fp8_f32 v27, v20, v21 op_sel:[0,0,1]
	v_add_co_u32_e32 v20, vcc, s60, v18
	v_fmamk_f32 v15, v47, 0x3c800000, v15
	s_nop 0
	v_addc_co_u32_e32 v21, vcc, 0, v19, vcc
	v_min_f32_e32 v14, 0x40e00000, v14
	v_min_f32_e32 v15, 0x40e00000, v15
	global_store_dwordx2 v[20:21], v[26:27], off
	v_mul_f32_e32 v20, 0xc01d265f, v14
	v_mul_f32_e32 v21, 0xc01d265f, v15
	v_exp_f32_e32 v20, v20
	v_exp_f32_e32 v21, v21
	v_fmamk_f32 v16, v48, 0x3c800000, v16
	v_fmac_f32_e32 v17, 0x3c800000, v49
	v_min_f32_e32 v16, 0x40e00000, v16
	v_min_f32_e32 v17, 0x40e00000, v17
	v_mul_f32_e32 v22, 0xc01d265f, v16
	v_mul_f32_e32 v23, 0xc01d265f, v17
	v_add_f32_e32 v20, 1.0, v20
	v_add_f32_e32 v21, 1.0, v21
	v_exp_f32_e32 v22, v22
	v_exp_f32_e32 v23, v23
	v_rcp_f32_e32 v20, v20
	v_rcp_f32_e32 v21, v21
	v_fmamk_f32 v10, v42, 0x3c800000, v10
	v_fmamk_f32 v11, v43, 0x3c800000, v11
	v_med3_f32 v10, v10, s57, v200
	v_med3_f32 v11, v11, s57, v200
	v_add_f32_e32 v22, 1.0, v22
	v_add_f32_e32 v23, 1.0, v23
	v_fmamk_f32 v6, v38, 0x3c800000, v6
	v_fmamk_f32 v7, v39, 0x3c800000, v7
	v_rcp_f32_e32 v22, v22
	v_rcp_f32_e32 v23, v23
	v_pk_add_f32 v[10:11], v[10:11], 1.0 op_sel_hi:[1,0]
	v_pk_mul_f32 v[14:15], v[14:15], v[20:21]
	v_min_f32_e32 v6, 0x40e00000, v6
	v_min_f32_e32 v7, 0x40e00000, v7
	v_pk_mul_f32 v[10:11], v[10:11], v[14:15]
	v_mul_f32_e32 v14, 0xc01d265f, v6
	v_mul_f32_e32 v15, 0xc01d265f, v7
	v_fmamk_f32 v12, v44, 0x3c800000, v12
	v_fmac_f32_e32 v13, 0x3c800000, v45
	v_exp_f32_e32 v14, v14
	v_exp_f32_e32 v15, v15
	v_med3_f32 v12, v12, s57, v200
	v_med3_f32 v13, v13, s57, v200
	v_fmamk_f32 v8, v40, 0x3c800000, v8
	v_fmac_f32_e32 v9, 0x3c800000, v41
	v_pk_add_f32 v[12:13], v[12:13], 1.0 op_sel_hi:[1,0]
	v_pk_mul_f32 v[16:17], v[16:17], v[22:23]
	v_min_f32_e32 v8, 0x40e00000, v8
	v_min_f32_e32 v9, 0x40e00000, v9
	v_pk_mul_f32 v[12:13], v[12:13], v[16:17]
	v_mul_f32_e32 v16, 0xc01d265f, v8
	v_mul_f32_e32 v17, 0xc01d265f, v9
	v_add_f32_e32 v14, 1.0, v14
	v_add_f32_e32 v15, 1.0, v15
	v_exp_f32_e32 v16, v16
	v_exp_f32_e32 v17, v17
	v_rcp_f32_e32 v14, v14
	v_rcp_f32_e32 v15, v15
	v_fmamk_f32 v2, v34, 0x3c800000, v2
	v_fmamk_f32 v3, v35, 0x3c800000, v3
	v_med3_f32 v2, v2, s57, v200
	v_med3_f32 v3, v3, s57, v200
	v_add_f32_e32 v16, 1.0, v16
	v_add_f32_e32 v17, 1.0, v17
	v_rcp_f32_e32 v16, v16
	v_rcp_f32_e32 v17, v17
	v_pk_add_f32 v[2:3], v[2:3], 1.0 op_sel_hi:[1,0]
	v_pk_mul_f32 v[6:7], v[6:7], v[14:15]
	v_fmamk_f32 v4, v36, 0x3c800000, v4
	v_pk_mul_f32 v[2:3], v[2:3], v[6:7]
	v_mov_b32_e32 v6, v163
	v_mov_b32_e32 v7, v163
	v_fmac_f32_e32 v5, 0x3c800000, v37
	v_cvt_pk_fp8_f32 v6, v10, v11
	v_cvt_pk_fp8_f32 v7, v2, v3
	v_med3_f32 v4, v4, s57, v200
	v_med3_f32 v5, v5, s57, v200
	v_pk_add_f32 v[4:5], v[4:5], 1.0 op_sel_hi:[1,0]
	v_pk_mul_f32 v[2:3], v[8:9], v[16:17]
	v_cvt_pk_fp8_f32 v6, v12, v13 op_sel:[0,0,1]
	v_pk_mul_f32 v[2:3], v[4:5], v[2:3]
	s_nop 0
	v_cvt_pk_fp8_f32 v7, v2, v3 op_sel:[0,0,1]
	v_add_co_u32_e32 v2, vcc, 0x58000, v18
	s_nop 1
	v_addc_co_u32_e32 v3, vcc, 0, v19, vcc
	s_and_b64 vcc, exec, s[4:5]
	s_mov_b64 s[4:5], -1
	global_store_dwordx2 v[2:3], v[6:7], off
	s_cbranch_vccnz .LBB0_982
	s_andn2_b64 vcc, exec, s[18:19]
	s_cbranch_vccnz .LBB0_981
	s_barrier
	s_branch .LBB0_981
.LBB0_1002:
	s_mov_b64 s[98:99], exec
	s_mov_b64 exec, -1
	v_mbcnt_lo_u32_b32 v190, -1, 0
	s_mov_b64 exec, s[98:99]
	s_waitcnt vmcnt(0)
	s_barrier

;     __device__ __forceinline__ void operator()(const f32x4 (&acc)[2][2][4][2], const Unit& u, int wr, int wc, int fr, int fq) const {
;         const int row0 = u.pm * BM + wr * 64 + fr; const int colt = (u.pn % ntile_mod) * BM;
;         const int col0 = colt + wc * 32 + 8 * fq, bcol0 = u.pn * BM + wc * 32 + 8 * fq;
;         f32x4 bv[2][2];
; #pragma unroll
;         for (int bj = 0; bj < 2; ++bj)
; #pragma unroll
;             for (int n = 0; n < 2; ++n) bv[bj][n] = bias ? *(const f32x4*)(bias + bcol0 + bj * HALF + 4 * n) : (f32x4){0.f, 0.f, 0.f, 0.f};
.LBB0_1072:
	v_lshl_or_b32 v2, s52, 8, v195
	v_ashrrev_i32_e32 v3, 31, v2
	v_lshl_add_u64 v[2:3], v[2:3], 2, s[24:25]
	v_mov_b32_e32 v240, 0
	v_mov_b32_e32 v241, 0
	v_mov_b32_e32 v242, 0
	v_mov_b32_e32 v243, 0
	v_mov_b32_e32 v248, 0
	v_mov_b32_e32 v249, 0
	v_mov_b32_e32 v250, 0
	v_mov_b32_e32 v251, 0
	v_mov_b32_e32 v252, 0
	v_mov_b32_e32 v253, 0
	v_mov_b32_e32 v254, 0
	v_mov_b32_e32 v255, 0
	v_mov_b32_e32 v244, 0
	v_mov_b32_e32 v245, 0
	v_mov_b32_e32 v247, 0
	v_mov_b32_e32 v205, 0
	s_cmp_eq_u64 s[24:25], 0
	s_cbranch_scc1 .Lb10_nobias
	global_load_dwordx4 v[240:243], v[2:3], off
	global_load_dwordx4 v[248:251], v[2:3], off offset:16
	global_load_dwordx4 v[252:255], v[2:3], off offset:512
	global_load_dwordx2 v[244:245], v[2:3], off offset:528
	global_load_dword v247, v[2:3], off offset:536
	global_load_dword v205, v[2:3], off offset:540

; __device__ __forceinline__ unsigned cvt_pk_bf16(float lo, float hi) { unsigned r; asm volatile("v_cvt_pk_bf16_f32 %0, %1, %2" : "=v"(r) : "v"(lo), "v"(hi)); return r; }
;     __device__ __forceinline__ void operator()(const f32x4 (&acc)[2][2][4][2], const Unit& u, int wr, int wc, int fr, int fq) const {
;         const int row0 = u.pm * BM + wr * 64 + fr; const int colt = (u.pn % ntile_mod) * BM;
;         const int col0 = colt + wc * 32 + 8 * fq, bcol0 = u.pn * BM + wc * 32 + 8 * fq;
;         f32x4 bv[2][2];
; #pragma unroll
;         for (int bj = 0; bj < 2; ++bj)
; #pragma unroll
;             for (int n = 0; n < 2; ++n) bv[bj][n] = bias ? *(const f32x4*)(bias + bcol0 + bj * HALF + 4 * n) : (f32x4){0.f, 0.f, 0.f, 0.f};
; #pragma unroll
;         for (int ai = 0; ai < 2; ++ai)
; #pragma unroll
;             for (int m = 0; m < 4; ++m) { bf16_t* rowp = O + (size_t)(row0 + ai * HALF + m * 16) * ldc + col0;
; #pragma unroll
;                 for (int bj = 0; bj < 2; ++bj) { const f32x4 v0 = acc[ai][bj][m][0] * scale + bv[bj][0], v1 = acc[ai][bj][m][1] * scale + bv[bj][1];
;                     u32x4 w; w.x = cvt_pk_bf16(v0[0], v0[1]); w.y = cvt_pk_bf16(v0[2], v0[3]); w.z = cvt_pk_bf16(v1[0], v1[1]); w.w = cvt_pk_bf16(v1[2], v1[3]);
;                     *(u32x4*)(rowp + bj * HALF) = w; } }
.LBB0_1076:
	v_mov_b64_e32 v[6:7], v[240:241]
	v_mov_b64_e32 v[8:9], v[242:243]
	v_mov_b64_e32 v[2:3], v[248:249]
	v_mov_b64_e32 v[4:5], v[250:251]
	v_mov_b64_e32 v[14:15], v[252:253]
	v_mov_b64_e32 v[16:17], v[254:255]
	v_mov_b64_e32 v[10:11], v[244:245]
	v_mov_b32_e32 v12, v247
	v_mov_b32_e32 v13, v205
.LBB0_1084:
	s_ashr_i32 s4, s52, 31
	s_lshr_b32 s4, s4, 29
	s_add_i32 s4, s52, s4
	s_and_b32 s4, s4, 0xfffff8
	s_sub_i32 s4, s52, s4
	v_lshl_add_u32 v24, s67, 8, v169
	v_lshl_or_b32 v18, s4, 8, v195
	v_ashrrev_i32_e32 v25, 31, v24
	v_ashrrev_i32_e32 v19, 31, v18
	v_lshlrev_b64 v[20:21], 12, v[24:25]
	v_lshl_add_u64 v[20:21], s[16:17], 0, v[20:21]
	v_lshlrev_b64 v[26:27], 1, v[18:19]
	v_lshl_add_u64 v[18:19], v[20:21], 0, v[26:27]
	v_pk_fma_f32 v[20:21], v[158:159], s[38:39], v[6:7] op_sel_hi:[1,0,1]
	v_pk_fma_f32 v[22:23], v[160:161], s[38:39], v[8:9] op_sel_hi:[1,0,1]
	v_cvt_pk_bf16_f32 v20, v20, v21
	v_pk_fma_f32 v[28:29], v[156:157], s[38:39], v[4:5] op_sel_hi:[1,0,1]
	v_cvt_pk_bf16_f32 v21, v22, v23
	v_pk_fma_f32 v[30:31], v[154:155], s[38:39], v[2:3] op_sel_hi:[1,0,1]
	v_pk_fma_f32 v[32:33], v[138:139], s[38:39], v[2:3] op_sel_hi:[1,0,1]
	v_cvt_pk_bf16_f32 v22, v30, v31
	v_cvt_pk_bf16_f32 v23, v28, v29
	global_store_dwordx4 v[18:19], v[20:23], off
	v_pk_fma_f32 v[28:29], v[144:145], s[38:39], v[12:13] op_sel_hi:[1,0,1]
	v_pk_fma_f32 v[30:31], v[142:143], s[38:39], v[10:11] op_sel_hi:[1,0,1]
	v_pk_fma_f32 v[20:21], v[150:151], s[38:39], v[14:15] op_sel_hi:[1,0,1]
	v_pk_fma_f32 v[22:23], v[152:153], s[38:39], v[16:17] op_sel_hi:[1,0,1]
	v_cvt_pk_bf16_f32 v20, v20, v21
	s_nop 0
	v_cvt_pk_bf16_f32 v21, v22, v23
	v_cvt_pk_bf16_f32 v22, v30, v31
	v_cvt_pk_bf16_f32 v23, v28, v29
	global_store_dwordx4 v[18:19], v[20:23], off offset:256
	v_pk_fma_f32 v[30:31], v[140:141], s[38:39], v[4:5] op_sel_hi:[1,0,1]
	s_nop 0
	v_or_b32_e32 v20, 16, v24
	v_ashrrev_i32_e32 v21, 31, v20
	v_lshlrev_b64 v[20:21], 12, v[20:21]
	v_lshl_add_u64 v[20:21], s[16:17], 0, v[20:21]
	v_lshl_add_u64 v[28:29], v[20:21], 0, v[26:27]
	v_pk_fma_f32 v[20:21], v[146:147], s[38:39], v[6:7] op_sel_hi:[1,0,1]
	v_pk_fma_f32 v[22:23], v[148:149], s[38:39], v[8:9] op_sel_hi:[1,0,1]
	v_cvt_pk_bf16_f32 v20, v20, v21
	s_nop 0
	v_cvt_pk_bf16_f32 v21, v22, v23
	v_cvt_pk_bf16_f32 v22, v32, v33
	v_cvt_pk_bf16_f32 v23, v30, v31
	global_store_dwordx4 v[28:29], v[20:23], off
	v_pk_fma_f32 v[30:31], v[128:129], s[38:39], v[12:13] op_sel_hi:[1,0,1]
	v_pk_fma_f32 v[32:33], v[126:127], s[38:39], v[10:11] op_sel_hi:[1,0,1]
	v_pk_fma_f32 v[20:21], v[134:135], s[38:39], v[14:15] op_sel_hi:[1,0,1]
	v_pk_fma_f32 v[22:23], v[136:137], s[38:39], v[16:17] op_sel_hi:[1,0,1]
	v_cvt_pk_bf16_f32 v20, v20, v21
	s_nop 0
	v_cvt_pk_bf16_f32 v21, v22, v23
	v_cvt_pk_bf16_f32 v22, v32, v33
	v_cvt_pk_bf16_f32 v23, v30, v31
	global_store_dwordx4 v[28:29], v[20:23], off offset:256
	v_pk_fma_f32 v[30:31], v[124:125], s[38:39], v[4:5] op_sel_hi:[1,0,1]
	v_pk_fma_f32 v[32:33], v[122:123], s[38:39], v[2:3] op_sel_hi:[1,0,1]
	v_or_b32_e32 v20, 32, v24
	v_ashrrev_i32_e32 v21, 31, v20
	v_lshlrev_b64 v[20:21], 12, v[20:21]
	v_lshl_add_u64 v[20:21], s[16:17], 0, v[20:21]
	v_lshl_add_u64 v[28:29], v[20:21], 0, v[26:27]
	v_pk_fma_f32 v[20:21], v[130:131], s[38:39], v[6:7] op_sel_hi:[1,0,1]
	v_pk_fma_f32 v[22:23], v[132:133], s[38:39], v[8:9] op_sel_hi:[1,0,1]
	v_cvt_pk_bf16_f32 v20, v20, v21
	s_nop 0
	v_cvt_pk_bf16_f32 v21, v22, v23
	v_cvt_pk_bf16_f32 v22, v32, v33
	v_cvt_pk_bf16_f32 v23, v30, v31
	global_store_dwordx4 v[28:29], v[20:23], off
	v_pk_fma_f32 v[30:31], v[112:113], s[38:39], v[12:13] op_sel_hi:[1,0,1]
	v_pk_fma_f32 v[32:33], v[110:111], s[38:39], v[10:11] op_sel_hi:[1,0,1]
	v_pk_fma_f32 v[20:21], v[118:119], s[38:39], v[14:15] op_sel_hi:[1,0,1]
	v_pk_fma_f32 v[22:23], v[120:121], s[38:39], v[16:17] op_sel_hi:[1,0,1]
	v_cvt_pk_bf16_f32 v20, v20, v21
	s_nop 0
	v_cvt_pk_bf16_f32 v21, v22, v23
	v_cvt_pk_bf16_f32 v22, v32, v33
	v_cvt_pk_bf16_f32 v23, v30, v31
	global_store_dwordx4 v[28:29], v[20:23], off offset:256
	v_pk_fma_f32 v[28:29], v[106:107], s[38:39], v[2:3] op_sel_hi:[1,0,1]
	s_nop 0
	v_or_b32_e32 v20, 48, v24
	v_ashrrev_i32_e32 v21, 31, v20
	v_lshlrev_b64 v[20:21], 12, v[20:21]
	v_lshl_add_u64 v[20:21], s[16:17], 0, v[20:21]
	v_lshl_add_u64 v[24:25], v[20:21], 0, v[26:27]
	v_pk_fma_f32 v[22:23], v[116:117], s[38:39], v[8:9] op_sel_hi:[1,0,1]
	v_pk_fma_f32 v[20:21], v[114:115], s[38:39], v[6:7] op_sel_hi:[1,0,1]
	v_pk_fma_f32 v[26:27], v[108:109], s[38:39], v[4:5] op_sel_hi:[1,0,1]
	v_cvt_pk_bf16_f32 v20, v20, v21
	v_cvt_pk_bf16_f32 v21, v22, v23
	v_cvt_pk_bf16_f32 v22, v28, v29
	v_pk_fma_f32 v[28:29], v[98:99], s[38:39], v[10:11] op_sel_hi:[1,0,1]
	v_cvt_pk_bf16_f32 v23, v26, v27
	global_store_dwordx4 v[24:25], v[20:23], off
	v_pk_fma_f32 v[26:27], v[100:101], s[38:39], v[12:13] op_sel_hi:[1,0,1]
; __device__ __forceinline__ unsigned cvt_pk_bf16(float lo, float hi) { unsigned r; asm volatile("v_cvt_pk_bf16_f32 %0, %1, %2" : "=v"(r) : "v"(lo), "v"(hi)); return r; }
;     __device__ __forceinline__ void operator()(const f32x4 (&acc)[2][2][4][2], const Unit& u, int wr, int wc, int fr, int fq) const {
;     ...
;         for (int ai = 0; ai < 2; ++ai)
; #pragma unroll
;             for (int m = 0; m < 4; ++m) { bf16_t* rowp = O + (size_t)(row0 + ai * HALF + m * 16) * ldc + col0;
; #pragma unroll
;                 for (int bj = 0; bj < 2; ++bj) { const f32x4 v0 = acc[ai][bj][m][0] * scale + bv[bj][0], v1 = acc[ai][bj][m][1] * scale + bv[bj][1];
;                     u32x4 w; w.x = cvt_pk_bf16(v0[0], v0[1]); w.y = cvt_pk_bf16(v0[2], v0[3]); w.z = cvt_pk_bf16(v1[0], v1[1]); w.w = cvt_pk_bf16(v1[2], v1[3]);
;                     *(u32x4*)(rowp + bj * HALF) = w; } }
	s_nop 0
	v_pk_fma_f32 v[22:23], v[104:105], s[38:39], v[16:17] op_sel_hi:[1,0,1]
	v_pk_fma_f32 v[20:21], v[102:103], s[38:39], v[14:15] op_sel_hi:[1,0,1]
	s_nop 0
	v_cvt_pk_bf16_f32 v20, v20, v21
	v_cvt_pk_bf16_f32 v21, v22, v23
	v_cvt_pk_bf16_f32 v22, v28, v29
	v_cvt_pk_bf16_f32 v23, v26, v27
	global_store_dwordx4 v[24:25], v[20:23], off offset:256
	v_pk_fma_f32 v[26:27], v[92:93], s[38:39], v[4:5] op_sel_hi:[1,0,1]
	v_pk_fma_f32 v[28:29], v[90:91], s[38:39], v[2:3] op_sel_hi:[1,0,1]
	v_pk_fma_f32 v[22:23], v[96:97], s[38:39], v[8:9] op_sel_hi:[1,0,1]
	v_pk_fma_f32 v[20:21], v[94:95], s[38:39], v[6:7] op_sel_hi:[1,0,1]
	v_lshl_add_u64 v[24:25], v[18:19], 0, s[40:41]
	v_cvt_pk_bf16_f32 v20, v20, v21
	v_cvt_pk_bf16_f32 v21, v22, v23
	v_cvt_pk_bf16_f32 v22, v28, v29
	v_cvt_pk_bf16_f32 v23, v26, v27
	v_add_co_u32_e32 v26, vcc, s62, v18
	v_pk_fma_f32 v[28:29], v[78:79], s[38:39], v[10:11] op_sel_hi:[1,0,1]
	s_nop 0
	v_addc_co_u32_e32 v27, vcc, 0, v19, vcc
	global_store_dwordx4 v[26:27], v[20:23], off
	v_pk_fma_f32 v[26:27], v[80:81], s[38:39], v[12:13] op_sel_hi:[1,0,1]
	s_nop 0
	v_pk_fma_f32 v[22:23], v[88:89], s[38:39], v[16:17] op_sel_hi:[1,0,1]
	v_pk_fma_f32 v[20:21], v[86:87], s[38:39], v[14:15] op_sel_hi:[1,0,1]
	s_nop 0
	v_cvt_pk_bf16_f32 v20, v20, v21
	v_cvt_pk_bf16_f32 v21, v22, v23
	v_cvt_pk_bf16_f32 v22, v28, v29
	v_cvt_pk_bf16_f32 v23, v26, v27
	global_store_dwordx4 v[24:25], v[20:23], off offset:256
	v_pk_fma_f32 v[26:27], v[76:77], s[38:39], v[4:5] op_sel_hi:[1,0,1]
	v_pk_fma_f32 v[28:29], v[74:75], s[38:39], v[2:3] op_sel_hi:[1,0,1]
	v_pk_fma_f32 v[22:23], v[84:85], s[38:39], v[8:9] op_sel_hi:[1,0,1]
	v_pk_fma_f32 v[20:21], v[82:83], s[38:39], v[6:7] op_sel_hi:[1,0,1]
	v_lshl_add_u64 v[24:25], v[18:19], 0, s[42:43]
	v_cvt_pk_bf16_f32 v20, v20, v21
	v_cvt_pk_bf16_f32 v21, v22, v23
	v_cvt_pk_bf16_f32 v22, v28, v29
	v_cvt_pk_bf16_f32 v23, v26, v27
	v_add_co_u32_e32 v26, vcc, s63, v18
	v_pk_fma_f32 v[28:29], v[62:63], s[38:39], v[10:11] op_sel_hi:[1,0,1]
	s_nop 0
	v_addc_co_u32_e32 v27, vcc, 0, v19, vcc
	global_store_dwordx4 v[26:27], v[20:23], off
	v_pk_fma_f32 v[26:27], v[64:65], s[38:39], v[12:13] op_sel_hi:[1,0,1]
	s_nop 0
	v_pk_fma_f32 v[22:23], v[72:73], s[38:39], v[16:17] op_sel_hi:[1,0,1]
	v_pk_fma_f32 v[20:21], v[70:71], s[38:39], v[14:15] op_sel_hi:[1,0,1]
	s_nop 0
	v_cvt_pk_bf16_f32 v20, v20, v21
	v_cvt_pk_bf16_f32 v21, v22, v23
	v_cvt_pk_bf16_f32 v22, v28, v29
	v_cvt_pk_bf16_f32 v23, v26, v27
	global_store_dwordx4 v[24:25], v[20:23], off offset:256
	v_pk_fma_f32 v[26:27], v[60:61], s[38:39], v[4:5] op_sel_hi:[1,0,1]
	v_pk_fma_f32 v[28:29], v[58:59], s[38:39], v[2:3] op_sel_hi:[1,0,1]
	v_pk_fma_f32 v[22:23], v[68:69], s[38:39], v[8:9] op_sel_hi:[1,0,1]
	v_pk_fma_f32 v[20:21], v[66:67], s[38:39], v[6:7] op_sel_hi:[1,0,1]
	v_lshl_add_u64 v[24:25], v[18:19], 0, s[44:45]
	v_cvt_pk_bf16_f32 v20, v20, v21
	v_cvt_pk_bf16_f32 v21, v22, v23
	v_cvt_pk_bf16_f32 v22, v28, v29
	v_cvt_pk_bf16_f32 v23, v26, v27
	v_add_co_u32_e32 v26, vcc, s64, v18
	v_pk_fma_f32 v[28:29], v[46:47], s[38:39], v[10:11] op_sel_hi:[1,0,1]
	s_nop 0
	v_addc_co_u32_e32 v27, vcc, 0, v19, vcc
	global_store_dwordx4 v[26:27], v[20:23], off
	v_pk_fma_f32 v[26:27], v[48:49], s[38:39], v[12:13] op_sel_hi:[1,0,1]
	v_pk_fma_f32 v[6:7], v[50:51], s[38:39], v[6:7] op_sel_hi:[1,0,1]
	v_pk_fma_f32 v[22:23], v[56:57], s[38:39], v[16:17] op_sel_hi:[1,0,1]
	v_pk_fma_f32 v[20:21], v[54:55], s[38:39], v[14:15] op_sel_hi:[1,0,1]
	v_pk_fma_f32 v[8:9], v[52:53], s[38:39], v[8:9] op_sel_hi:[1,0,1]
	v_cvt_pk_bf16_f32 v20, v20, v21
	v_cvt_pk_bf16_f32 v21, v22, v23
	v_cvt_pk_bf16_f32 v22, v28, v29
	v_cvt_pk_bf16_f32 v23, v26, v27
	global_store_dwordx4 v[24:25], v[20:23], off offset:256
	s_nop 1
	v_pk_fma_f32 v[22:23], v[44:45], s[38:39], v[4:5] op_sel_hi:[1,0,1]
	v_pk_fma_f32 v[4:5], v[42:43], s[38:39], v[2:3] op_sel_hi:[1,0,1]
	v_cvt_pk_bf16_f32 v2, v6, v7
	v_add_co_u32_e32 v6, vcc, s65, v18
	v_cvt_pk_bf16_f32 v3, v8, v9
	v_cvt_pk_bf16_f32 v4, v4, v5
	v_cvt_pk_bf16_f32 v5, v22, v23
	v_lshl_add_u64 v[20:21], v[18:19], 0, s[46:47]
	s_nop 0
	v_addc_co_u32_e32 v7, vcc, 0, v19, vcc
	global_store_dwordx4 v[6:7], v[2:5], off
	s_and_b64 vcc, exec, s[2:3]
	s_mov_b64 s[2:3], -1
	v_pk_fma_f32 v[4:5], v[40:41], s[38:39], v[16:17] op_sel_hi:[1,0,1]
	v_pk_fma_f32 v[2:3], v[38:39], s[38:39], v[14:15] op_sel_hi:[1,0,1]
	v_pk_fma_f32 v[6:7], v[36:37], s[38:39], v[12:13] op_sel_hi:[1,0,1]
	v_pk_fma_f32 v[8:9], v[34:35], s[38:39], v[10:11] op_sel_hi:[1,0,1]
	v_cvt_pk_bf16_f32 v2, v2, v3
	v_cvt_pk_bf16_f32 v3, v4, v5
	s_nop 0
	v_cvt_pk_bf16_f32 v4, v8, v9
	v_cvt_pk_bf16_f32 v5, v6, v7
	global_store_dwordx4 v[20:21], v[2:5], off offset:256
	s_cbranch_vccnz .LBB0_1067
	s_andn2_b64 vcc, exec, s[14:15]
	s_cbranch_vccnz .LBB0_1066
	s_barrier
	s_branch .LBB0_1066

; __global__ void __launch_bounds__(NWAVES * 64, 2) fwd(Args args) {
	.amdhsa_kernel _Z3fwd4Args
		.amdhsa_group_segment_fixed_size 0
		.amdhsa_private_segment_fixed_size 0
		.amdhsa_kernarg_size 472
		.amdhsa_user_sgpr_count 2
		.amdhsa_user_sgpr_dispatch_ptr 0
		.amdhsa_user_sgpr_queue_ptr 0
		.amdhsa_user_sgpr_kernarg_segment_ptr 1
		.amdhsa_user_sgpr_dispatch_id 0
		.amdhsa_user_sgpr_kernarg_preload_length 0
		.amdhsa_user_sgpr_kernarg_preload_offset 0
		.amdhsa_user_sgpr_private_segment_size 0
		.amdhsa_uses_dynamic_stack 0
		.amdhsa_enable_private_segment 0
		.amdhsa_system_sgpr_workgroup_id_x 1
		.amdhsa_system_sgpr_workgroup_id_y 0
		.amdhsa_system_sgpr_workgroup_id_z 0
		.amdhsa_system_sgpr_workgroup_info 0
		.amdhsa_system_vgpr_workitem_id 0
		.amdhsa_next_free_vgpr 256
		.amdhsa_next_free_sgpr 102
		.amdhsa_accum_offset 256
		.amdhsa_reserve_vcc 1
		.amdhsa_float_round_mode_32 0
		.amdhsa_float_round_mode_16_64 0
		.amdhsa_float_denorm_mode_32 3
		.amdhsa_float_denorm_mode_16_64 3
		.amdhsa_dx10_clamp 1
		.amdhsa_ieee_mode 1
		.amdhsa_fp16_overflow 0
		.amdhsa_tg_split 0
		.amdhsa_exception_fp_ieee_invalid_op 0
		.amdhsa_exception_fp_denorm_src 0
		.amdhsa_exception_fp_ieee_div_zero 0
		.amdhsa_exception_fp_ieee_overflow 0
		.amdhsa_exception_fp_ieee_underflow 0
		.amdhsa_exception_fp_ieee_inexact 0
		.amdhsa_exception_int_div_zero 0
	.end_amdhsa_kernel

; __global__ void __launch_bounds__(NWAVES * 64, 2) fwd(Args args) {
amdhsa.kernels:
  - .agpr_count:     0
    .args:
      - .offset:         0
        .size:           216
        .value_kind:     by_value
      - .offset:         216
        .size:           4
        .value_kind:     hidden_block_count_x
      - .offset:         220
        .size:           4
        .value_kind:     hidden_block_count_y
      - .offset:         224
        .size:           4
        .value_kind:     hidden_block_count_z
      - .offset:         228
        .size:           2
        .value_kind:     hidden_group_size_x
      - .offset:         230
        .size:           2
        .value_kind:     hidden_group_size_y
      - .offset:         232
        .size:           2
        .value_kind:     hidden_group_size_z
      - .offset:         234
        .size:           2
        .value_kind:     hidden_remainder_x
      - .offset:         236
        .size:           2
        .value_kind:     hidden_remainder_y
      - .offset:         238
        .size:           2
        .value_kind:     hidden_remainder_z
      - .offset:         256
        .size:           8
        .value_kind:     hidden_global_offset_x
      - .offset:         264
        .size:           8
        .value_kind:     hidden_global_offset_y
      - .offset:         272
        .size:           8
        .value_kind:     hidden_global_offset_z
      - .offset:         280
        .size:           2
        .value_kind:     hidden_grid_dims
      - .offset:         336
        .size:           4
        .value_kind:     hidden_dynamic_lds_size
    .group_segment_fixed_size: 0
    .kernarg_segment_align: 8
    .kernarg_segment_size: 472
    .language:       OpenCL C
    .language_version:
      - 2
      - 0
    .max_flat_workgroup_size: 512
    .name:           _Z3fwd4Args
    .private_segment_fixed_size: 0
    .sgpr_count:     108
    .sgpr_spill_count: 58
    .symbol:         _Z3fwd4Args.kd
    .uniform_work_group_size: 1
    .uses_dynamic_stack: false
    .vgpr_count:     256
    .vgpr_spill_count: 0
    .wavefront_size: 64
